# loop-edge edit: a block-major step followed by another one takes a short back edge (pointer increments, barrier, j += 2) instead of the compiled loop bottom, loop top and hook
# speedup vs baseline: 1.0122x; 1.0122x over previous
; __device__ __forceinline__ void nsa_unit(unsigned char* ws, LAS unsigned char* lds, const LAS float* lut, int b, int g, int tau, int tid_in) {
;     ...
;         SLC_LOOP(false);
.LBB0_1185:
	s_cmp_lt_u32 s75, 2
	s_cbranch_scc1 .Lbm_old
	s_cmp_gt_i32 s75, s26
	s_cbranch_scc0 .Lbm_step
	s_cmp_eq_u32 s98, 0
	s_cbranch_scc1 .Lbm_old
	s_lshr_b32 s11, s75, 5
	s_lshl_b32 s11, s11, 2
	v_add_u32_e32 v78, s11, v165
	ds_read2_b32 v[174:175], v78 offset1:16
	s_mul_i32 s11, s91, 8320
	v_mul_u32_u24_e32 v79, 260, v250
	v_add3_u32 v79, v79, s11, v248
	v_lshlrev_b32_e32 v80, 6, v186
	v_sub_u32_e32 v80, v79, v80
	ds_read_b32 v70, v79 offset:0
	ds_read_b32 v71, v79 offset:16
	ds_read_b32 v72, v79 offset:32
	ds_read_b32 v73, v79 offset:48
	ds_read_b32 v66, v79 offset:256
	ds_read_b32 v67, v79 offset:272
	ds_read_b32 v68, v79 offset:288
	ds_read_b32 v69, v79 offset:304
	ds_read_b32 v62, v79 offset:512
	ds_read_b32 v63, v79 offset:528
	ds_read_b32 v64, v79 offset:544
	ds_read_b32 v65, v79 offset:560
	s_waitcnt lgkmcnt(0)
	ds_read_b32 v54, v79 offset:768
	ds_read_b32 v55, v79 offset:784
	ds_read_b32 v56, v79 offset:800
	ds_read_b32 v57, v79 offset:816
	ds_read_b32 v50, v79 offset:4160
	ds_read_b32 v51, v79 offset:4176
	ds_read_b32 v52, v79 offset:4192
	ds_read_b32 v53, v79 offset:4208
	ds_read_b32 v46, v79 offset:4416
	ds_read_b32 v47, v79 offset:4432
	ds_read_b32 v48, v79 offset:4448
	ds_read_b32 v49, v79 offset:4464
	s_waitcnt lgkmcnt(0)
	ds_read_b32 v42, v79 offset:4672
	ds_read_b32 v43, v79 offset:4688
	ds_read_b32 v44, v79 offset:4704
	ds_read_b32 v45, v79 offset:4720
	ds_read_b32 v38, v79 offset:4928
	ds_read_b32 v39, v79 offset:4944
	ds_read_b32 v40, v79 offset:4960
	ds_read_b32 v41, v79 offset:4976
	ds_read_b32 v74, v80 offset:1024
	ds_read_b32 v58, v80 offset:5184
	s_waitcnt lgkmcnt(0)
	v_mov_b32_e32 v75, v74
	v_mov_b32_e32 v76, v74
	v_mov_b32_e32 v77, v74
	v_mov_b32_e32 v59, v58
	v_mov_b32_e32 v60, v58
	v_mov_b32_e32 v61, v58
	s_bitcmp1_b32 s26, 0
	s_cbranch_scc1 .Lbm_hk4
	s_waitcnt vmcnt(2)
	s_branch .Lbm_hkd

.Lbm_back:
	s_add_i32 s11, s75, 2
	s_cmp_gt_i32 s11, s26
	s_cbranch_scc1 .LBB0_1228
	s_add_u32 s64, s64, 0x10000
	s_addc_u32 s65, s65, 0
	s_add_u32 s62, s62, 0x100
	s_addc_u32 s63, s63, 0
	v_add_u32_e32 v196, 0x200, v196
	s_addk_i32 s1, 0x4000
	s_mov_b32 s75, s11
	s_add_i32 s76, s11, 2
	s_cmp_eq_u32 s99, 1
	s_cselect_b32 s99, 0, s99
	s_waitcnt lgkmcnt(0)
	s_barrier
	s_branch .Lbm_step
